# router pass A: all eight x1 rows of a wave requested before the first is used (three 16-register banks); loop header waits vmcnt(16) instead of draining its own stores
# baseline (speedup 1.0000x reference)
.Lp7_w_skip:
	s_barrier
	s_lshl_b32 s33, s56, 6
	v_add_u32_e32 v46, s33, v103
	v_ashrrev_i32_e32 v47, 31, v46
	v_or_b32_e32 v2, 1, v46
	v_lshlrev_b64 v[0:1], 11, v[46:47]
	v_ashrrev_i32_e32 v3, 31, v2
	v_lshl_add_u64 v[0:1], v[36:37], 0, v[0:1]
	v_lshlrev_b64 v[2:3], 11, v[2:3]
	v_lshl_add_u64 v[2:3], v[36:37], 0, v[2:3]
	global_load_dwordx2 v[48:49], v[0:1], off
	global_load_dwordx2 v[50:51], v[0:1], off offset:512
	global_load_dwordx2 v[54:55], v[0:1], off offset:1024
	global_load_dwordx2 v[82:83], v[0:1], off offset:1536
	global_load_dwordx2 v[52:53], v[2:3], off
	global_load_dwordx2 v[56:57], v[2:3], off offset:512
	global_load_dwordx2 v[58:59], v[2:3], off offset:1024
	global_load_dwordx2 v[60:61], v[2:3], off offset:1536
	v_mov_b32_e32 v210, 0x1000
	v_mov_b32_e32 v211, 0
	v_lshl_add_u64 v[204:205], v[210:211], 0, v[0:1]
	v_lshl_add_u64 v[206:207], v[210:211], 1, v[0:1]
	v_lshl_add_u64 v[208:209], v[210:211], 1, v[204:205]
	global_load_dwordx2 v[152:153], v[204:205], off
	global_load_dwordx2 v[154:155], v[204:205], off offset:512
	global_load_dwordx2 v[156:157], v[204:205], off offset:1024
	global_load_dwordx2 v[158:159], v[204:205], off offset:1536
	global_load_dwordx2 v[160:161], v[204:205], off offset:2048
	global_load_dwordx2 v[162:163], v[204:205], off offset:2560
	global_load_dwordx2 v[164:165], v[204:205], off offset:3072
	global_load_dwordx2 v[166:167], v[204:205], off offset:3584
	global_load_dwordx2 v[168:169], v[206:207], off
	global_load_dwordx2 v[170:171], v[206:207], off offset:512
	global_load_dwordx2 v[172:173], v[206:207], off offset:1024
	global_load_dwordx2 v[174:175], v[206:207], off offset:1536
	global_load_dwordx2 v[176:177], v[206:207], off offset:2048
	global_load_dwordx2 v[178:179], v[206:207], off offset:2560
	global_load_dwordx2 v[180:181], v[206:207], off offset:3072
	global_load_dwordx2 v[182:183], v[206:207], off offset:3584
	global_load_dwordx2 v[188:189], v[208:209], off
	global_load_dwordx2 v[190:191], v[208:209], off offset:512
	global_load_dwordx2 v[192:193], v[208:209], off offset:1024
	global_load_dwordx2 v[194:195], v[208:209], off offset:1536
	global_load_dwordx2 v[196:197], v[208:209], off offset:2048
	global_load_dwordx2 v[198:199], v[208:209], off offset:2560
	global_load_dwordx2 v[200:201], v[208:209], off offset:3072
	global_load_dwordx2 v[202:203], v[208:209], off offset:3584
	ds_read_b128 v[0:3], v101
	ds_read_b128 v[4:7], v101 offset:1024
	ds_read_b128 v[8:11], v102
	ds_read_b128 v[12:15], v102 offset:1024
	ds_read_b128 v[16:19], v101 offset:2048
	ds_read_b128 v[20:23], v101 offset:3072
	ds_read_b128 v[24:27], v102 offset:2048
	ds_read_b128 v[28:31], v102 offset:3072
	s_mov_b32 s34, 2
	v_mov_b32_e32 v34, v110
	s_branch .LBB0_652

.LBB0_652:
	s_cmp_lg_u32 s34, 8
	s_cselect_b32 s0, s34, 6
	s_waitcnt vmcnt(16)
	v_mov_b64_e32 v[68:69], v[48:49]
	v_add_u32_e32 v48, s0, v46
	v_ashrrev_i32_e32 v49, 31, v48
	v_mov_b64_e32 v[66:67], v[50:51]
	v_lshlrev_b64 v[50:51], 11, v[48:49]
	v_or_b32_e32 v48, 1, v48
	v_ashrrev_i32_e32 v49, 31, v48
	v_lshlrev_b64 v[48:49], 11, v[48:49]
	v_mov_b64_e32 v[70:71], v[60:61]
	v_mov_b64_e32 v[74:75], v[52:53]
	v_lshl_add_u64 v[52:53], v[36:37], 0, v[50:51]
	v_lshl_add_u64 v[60:61], v[36:37], 0, v[48:49]
	v_mov_b64_e32 v[64:65], v[54:55]
	v_mov_b64_e32 v[78:79], v[58:59]
	v_mov_b64_e32 v[72:73], v[56:57]
	s_cmp_eq_u32 s34, 2
	s_cbranch_scc0 .Lp7b_n0
	v_mov_b64_e32 v[48:49], v[152:153]
	v_mov_b64_e32 v[50:51], v[154:155]
	v_mov_b64_e32 v[54:55], v[156:157]
	v_mov_b64_e32 v[62:63], v[158:159]
	v_mov_b64_e32 v[52:53], v[160:161]
	v_mov_b64_e32 v[56:57], v[162:163]
	v_mov_b64_e32 v[58:59], v[164:165]
	v_mov_b64_e32 v[60:61], v[166:167]
	s_branch .Lp7b_done
.Lp7b_n0:
	s_cmp_eq_u32 s34, 4
	s_cbranch_scc0 .Lp7b_n1
	v_mov_b64_e32 v[48:49], v[168:169]
	v_mov_b64_e32 v[50:51], v[170:171]
	v_mov_b64_e32 v[54:55], v[172:173]
	v_mov_b64_e32 v[62:63], v[174:175]
	v_mov_b64_e32 v[52:53], v[176:177]
	v_mov_b64_e32 v[56:57], v[178:179]
	v_mov_b64_e32 v[58:59], v[180:181]
	v_mov_b64_e32 v[60:61], v[182:183]
	s_branch .Lp7b_done
.Lp7b_n1:
	s_cmp_eq_u32 s34, 6
	s_cbranch_scc0 .Lp7b_n2
	v_mov_b64_e32 v[48:49], v[188:189]
	v_mov_b64_e32 v[50:51], v[190:191]
	v_mov_b64_e32 v[54:55], v[192:193]
	v_mov_b64_e32 v[62:63], v[194:195]
	v_mov_b64_e32 v[52:53], v[196:197]
	v_mov_b64_e32 v[56:57], v[198:199]
	v_mov_b64_e32 v[58:59], v[200:201]
	v_mov_b64_e32 v[60:61], v[202:203]
	s_branch .Lp7b_done
.Lp7b_n2:
.Lp7b_done:
	v_cvt_f32_f16_sdwa v93, v74 dst_sel:DWORD dst_unused:UNUSED_PAD src0_sel:WORD_1
	v_cvt_f32_f16_sdwa v92, v68 dst_sel:DWORD dst_unused:UNUSED_PAD src0_sel:WORD_1
	v_cvt_f32_f16_sdwa v85, v72 dst_sel:DWORD dst_unused:UNUSED_PAD src0_sel:WORD_1
	v_cvt_f32_f16_sdwa v84, v66 dst_sel:DWORD dst_unused:UNUSED_PAD src0_sel:WORD_1
	v_cvt_f32_f16_e32 v91, v74
	v_cvt_f32_f16_e32 v90, v68
	v_cvt_f32_f16_e32 v81, v72
	v_cvt_f32_f16_e32 v80, v66
	v_cvt_f32_f16_e32 v95, v75
	v_cvt_f32_f16_e32 v94, v69
	v_cvt_f32_f16_e32 v87, v73
	v_cvt_f32_f16_e32 v86, v67
	v_cvt_f32_f16_sdwa v97, v75 dst_sel:DWORD dst_unused:UNUSED_PAD src0_sel:WORD_1
	v_cvt_f32_f16_sdwa v96, v69 dst_sel:DWORD dst_unused:UNUSED_PAD src0_sel:WORD_1
	v_cvt_f32_f16_sdwa v89, v73 dst_sel:DWORD dst_unused:UNUSED_PAD src0_sel:WORD_1
	v_cvt_f32_f16_sdwa v88, v67 dst_sel:DWORD dst_unused:UNUSED_PAD src0_sel:WORD_1
	v_cvt_f32_f16_e32 v73, v78
	v_cvt_f32_f16_e32 v72, v64
	v_cvt_f32_f16_sdwa v75, v78 dst_sel:DWORD dst_unused:UNUSED_PAD src0_sel:WORD_1
	v_cvt_f32_f16_sdwa v74, v64 dst_sel:DWORD dst_unused:UNUSED_PAD src0_sel:WORD_1
	v_cvt_f32_f16_e32 v76, v65
	v_cvt_f32_f16_sdwa v78, v65 dst_sel:DWORD dst_unused:UNUSED_PAD src0_sel:WORD_1
	v_pk_mul_f32 v[64:65], v[92:93], v[92:93]
	v_pk_mul_f32 v[66:67], v[84:85], v[84:85]
	v_pk_fma_f32 v[64:65], v[90:91], v[90:91], v[64:65]
	v_pk_fma_f32 v[66:67], v[80:81], v[80:81], v[66:67]
	v_cvt_f32_f16_e32 v77, v79
	v_pk_fma_f32 v[64:65], v[94:95], v[94:95], v[64:65]
	v_pk_fma_f32 v[66:67], v[86:87], v[86:87], v[66:67]
	v_cvt_f32_f16_sdwa v79, v79 dst_sel:DWORD dst_unused:UNUSED_PAD src0_sel:WORD_1
	v_pk_fma_f32 v[64:65], v[96:97], v[96:97], v[64:65]
	v_pk_fma_f32 v[66:67], v[88:89], v[88:89], v[66:67]
	v_cvt_f32_f16_e32 v69, v71
	v_pk_add_f32 v[64:65], v[64:65], v[66:67]
	v_pk_mul_f32 v[66:67], v[74:75], v[74:75]
	v_cvt_f32_f16_e32 v68, v83
	v_pk_fma_f32 v[66:67], v[72:73], v[72:73], v[66:67]
	v_cvt_f32_f16_sdwa v71, v71 dst_sel:DWORD dst_unused:UNUSED_PAD src0_sel:WORD_1
	v_pk_fma_f32 v[66:67], v[76:77], v[76:77], v[66:67]
	s_nop 0
	v_pk_fma_f32 v[66:67], v[78:79], v[78:79], v[66:67]
	s_nop 0
	v_pk_add_f32 v[128:129], v[64:65], v[66:67]
	v_cvt_f32_f16_sdwa v67, v70 dst_sel:DWORD dst_unused:UNUSED_PAD src0_sel:WORD_1
	v_cvt_f32_f16_sdwa v66, v82 dst_sel:DWORD dst_unused:UNUSED_PAD src0_sel:WORD_1
	v_cvt_f32_f16_e32 v65, v70
	v_cvt_f32_f16_e32 v64, v82
	v_cvt_f32_f16_sdwa v70, v83 dst_sel:DWORD dst_unused:UNUSED_PAD src0_sel:WORD_1
	v_pk_mul_f32 v[82:83], v[66:67], v[66:67]
	s_nop 0
	v_pk_fma_f32 v[82:83], v[64:65], v[64:65], v[82:83]
	s_nop 0
	v_pk_fma_f32 v[82:83], v[68:69], v[68:69], v[82:83]
	s_nop 0
	v_pk_fma_f32 v[82:83], v[70:71], v[70:71], v[82:83]
	s_nop 0
	v_pk_add_f32 v[82:83], v[128:129], v[82:83]
	ds_bpermute_b32 v128, v104, v82
	ds_bpermute_b32 v129, v104, v83
	s_waitcnt lgkmcnt(0)
	v_pk_add_f32 v[82:83], v[82:83], v[128:129]
	ds_bpermute_b32 v128, v105, v82
	ds_bpermute_b32 v129, v105, v83
	s_waitcnt lgkmcnt(0)
	v_pk_add_f32 v[82:83], v[82:83], v[128:129]
	ds_bpermute_b32 v128, v106, v82
	ds_bpermute_b32 v129, v106, v83
	s_waitcnt lgkmcnt(0)
	v_pk_add_f32 v[82:83], v[82:83], v[128:129]
	ds_bpermute_b32 v128, v107, v82
	ds_bpermute_b32 v129, v107, v83
	s_waitcnt lgkmcnt(0)
	v_pk_add_f32 v[82:83], v[82:83], v[128:129]
	ds_bpermute_b32 v128, v108, v82
	ds_bpermute_b32 v129, v108, v83
	s_waitcnt lgkmcnt(0)
	v_pk_add_f32 v[82:83], v[82:83], v[128:129]
	ds_bpermute_b32 v128, v109, v82
	ds_bpermute_b32 v129, v109, v83
	s_waitcnt lgkmcnt(0)
	v_pk_add_f32 v[82:83], v[82:83], v[128:129]
	s_nop 0
	v_pk_fma_f32 v[82:83], v[82:83], s[4:5], v[44:45] op_sel_hi:[1,0,0]
	s_nop 0
	v_mul_f32_e32 v47, 0x4b800000, v82
	v_cmp_gt_f32_e32 vcc, s49, v82
	v_cmp_gt_f32_e64 s[0:1], s49, v83
	s_nop 0
	v_cndmask_b32_e32 v47, v82, v47, vcc
	v_rsq_f32_e32 v82, v47
	v_mul_f32_e32 v47, 0x4b800000, v83
	v_cndmask_b32_e64 v47, v83, v47, s[0:1]
	v_rsq_f32_e32 v83, v47
	s_nop 0
	v_pk_mul_f32 v[128:129], v[82:83], s[30:31] op_sel_hi:[1,0]
	s_nop 0
	v_cndmask_b32_e64 v83, v83, v129, s[0:1]
	v_cndmask_b32_e32 v82, v82, v128, vcc
	s_and_saveexec_b64 s[0:1], s[10:11]
	s_cbranch_execz .LBB0_651
	ds_write_b64 v34, v[82:83]
	s_branch .LBB0_651
